# baseline (speedup 1.0000x reference)
.Lp1_smap_done:
	v_and_b32_e32 v94, 1, v99
	v_lshl_or_b32 v96, v94, 6, v103
	s_movk_i32 s100, 0x90
	v_mad_u32_u24 v88, v88, s100, v96
	v_mad_u32_u24 v90, v90, s100, v96
	v_mad_u32_u24 v92, v92, s100, v96
	v_lshl_add_u32 v86, v94, 12, v75
	s_movk_i32 s100, 0x1800
	v_mad_u32_u24 v96, v85, s100, v84
	ds_read_b128 v[40:43], v96
	ds_read_b128 v[44:47], v96 offset:1024
	ds_read_b128 v[48:51], v96 offset:2048
	ds_read_b128 v[52:55], v96 offset:3072
	ds_read_b128 v[56:59], v96 offset:4096
	ds_read_b128 v[60:63], v96 offset:5120
	s_lshr_b32 s101, s18, 8
	s_waitcnt lgkmcnt(0)
	s_mov_b32 s100, 0x3f596d27
	s_branch .LBB4_37

.LBB4_39:
	s_or_b64 exec, exec, s[32:33]
	s_setprio 1
	ds_read_b128 v[26:29], v86
	ds_read_b128 v[30:33], v86 offset:1024
	ds_read_b128 v[106:109], v86 offset:2048
	ds_read_b128 v[110:113], v86 offset:3072
	s_waitcnt lgkmcnt(2)
	v_mfma_f32_16x16x32_f16 v[34:37], v[26:29], v[40:43], 0
	v_mfma_f32_16x16x32_f16 v[114:117], v[26:29], v[48:51], 0
	v_mfma_f32_16x16x32_f16 v[118:121], v[26:29], v[56:59], 0
	v_mfma_f32_16x16x32_f16 v[34:37], v[30:33], v[44:47], v[34:37]
	v_mfma_f32_16x16x32_f16 v[114:117], v[30:33], v[52:55], v[114:117]
	v_mfma_f32_16x16x32_f16 v[118:121], v[30:33], v[60:63], v[118:121]
	s_waitcnt lgkmcnt(0)
	v_mfma_f32_16x16x32_f16 v[122:125], v[106:109], v[40:43], 0
	v_mfma_f32_16x16x32_f16 v[122:125], v[110:113], v[44:47], v[122:125]
	s_nop 2
	v_cvt_pk_f16_f32 v34, v34, v35
	v_cvt_pk_f16_f32 v35, v36, v37
	ds_write_b64 v88, v[34:35]
	v_cvt_pk_f16_f32 v114, v114, v115
	v_cvt_pk_f16_f32 v115, v116, v117
	ds_write_b64 v90, v[114:115]
	v_cvt_pk_f16_f32 v118, v118, v119
	v_cvt_pk_f16_f32 v119, v120, v121
	ds_write_b64 v92, v[118:119]
	v_mfma_f32_16x16x32_f16 v[34:37], v[106:109], v[48:51], 0
	v_mfma_f32_16x16x32_f16 v[114:117], v[106:109], v[56:59], 0
	v_mfma_f32_16x16x32_f16 v[34:37], v[110:113], v[52:55], v[34:37]
	v_mfma_f32_16x16x32_f16 v[114:117], v[110:113], v[60:63], v[114:117]
	v_cvt_pk_f16_f32 v122, v122, v123
	v_cvt_pk_f16_f32 v123, v124, v125
	ds_write_b64 v88, v[122:123] offset:32
	s_nop 3
	v_cvt_pk_f16_f32 v34, v34, v35
	v_cvt_pk_f16_f32 v35, v36, v37
	ds_write_b64 v90, v[34:35] offset:32
	v_cvt_pk_f16_f32 v114, v114, v115
	v_cvt_pk_f16_f32 v115, v116, v117
	ds_write_b64 v92, v[114:115] offset:32
	s_setprio 0
	s_waitcnt lgkmcnt(0)
	s_barrier
	v_add_u32_e32 v105, s25, v80
	ds_read_b128 v[30:33], v105
	ds_read_b128 v[34:37], v105 offset:64
	ds_read_b128 v[106:109], v105 offset:144
	ds_read_b128 v[110:113], v105 offset:208
	ds_read_b128 v[114:117], v105 offset:288
	ds_read_b128 v[122:125], v105 offset:352
	s_waitcnt lgkmcnt(4)
	v_pk_fma_f16 v118, v30, s36, 0
	v_pk_fma_f16 v119, v31, s37, 0
	v_pk_fma_f16 v120, v32, s38, 0
	v_pk_fma_f16 v121, v33, s39, 0
	v_pk_fma_f16 v26, v34, s72, 0
	v_pk_fma_f16 v27, v35, s73, 0
	v_pk_fma_f16 v28, v36, s74, 0
	v_pk_fma_f16 v29, v37, s75, 0
	ds_read_b128 v[30:33], v105 offset:2592
	ds_read_b128 v[34:37], v105 offset:2656
	s_waitcnt lgkmcnt(4)
	v_pk_fma_f16 v118, v106, s40, v118
	v_pk_fma_f16 v119, v107, s41, v119
	v_pk_fma_f16 v120, v108, s42, v120
	v_pk_fma_f16 v121, v109, s43, v121
	v_pk_fma_f16 v26, v110, s76, v26
	v_pk_fma_f16 v27, v111, s77, v27
	v_pk_fma_f16 v28, v112, s78, v28
	v_pk_fma_f16 v29, v113, s79, v29
	ds_read_b128 v[106:109], v105 offset:2736
	ds_read_b128 v[110:113], v105 offset:2800
	s_waitcnt lgkmcnt(4)
	v_pk_fma_f16 v118, v114, s44, v118
	v_pk_fma_f16 v119, v115, s45, v119
	v_pk_fma_f16 v120, v116, s46, v120
	v_pk_fma_f16 v121, v117, s47, v121
	v_pk_fma_f16 v26, v122, s80, v26
	v_pk_fma_f16 v27, v123, s81, v27
	v_pk_fma_f16 v28, v124, s82, v28
	v_pk_fma_f16 v29, v125, s83, v29
	ds_read_b128 v[114:117], v105 offset:2880
	ds_read_b128 v[122:125], v105 offset:2944
	s_waitcnt lgkmcnt(4)
	v_pk_fma_f16 v118, v30, s48, v118
	v_pk_fma_f16 v119, v31, s49, v119
	v_pk_fma_f16 v120, v32, s50, v120
	v_pk_fma_f16 v121, v33, s51, v121
	v_pk_fma_f16 v26, v34, s84, v26
	v_pk_fma_f16 v27, v35, s85, v27
	v_pk_fma_f16 v28, v36, s86, v28
	v_pk_fma_f16 v29, v37, s87, v29
	ds_read_b128 v[30:33], v105 offset:5184
	ds_read_b128 v[34:37], v105 offset:5248
	s_waitcnt lgkmcnt(4)
	v_pk_fma_f16 v118, v106, s52, v118
	v_pk_fma_f16 v119, v107, s53, v119
	v_pk_fma_f16 v120, v108, s54, v120
	v_pk_fma_f16 v121, v109, s55, v121
	v_pk_fma_f16 v26, v110, s88, v26
	v_pk_fma_f16 v27, v111, s89, v27
	v_pk_fma_f16 v28, v112, s90, v28
	v_pk_fma_f16 v29, v113, s91, v29
	ds_read_b128 v[106:109], v105 offset:5328
	ds_read_b128 v[110:113], v105 offset:5392
	s_waitcnt lgkmcnt(4)
	v_pk_fma_f16 v118, v114, s56, v118
	v_pk_fma_f16 v119, v115, s57, v119
	v_pk_fma_f16 v120, v116, s58, v120
	v_pk_fma_f16 v121, v117, s59, v121
	v_pk_fma_f16 v26, v122, s92, v26
	v_pk_fma_f16 v27, v123, s93, v27
	v_pk_fma_f16 v28, v124, s94, v28
	v_pk_fma_f16 v29, v125, s95, v29
	ds_read_b128 v[114:117], v105 offset:5472
	ds_read_b128 v[122:125], v105 offset:5536
	s_waitcnt lgkmcnt(4)
	v_pk_fma_f16 v118, v30, s60, v118
	v_pk_fma_f16 v119, v31, s61, v119
	v_pk_fma_f16 v120, v32, s62, v120
	v_pk_fma_f16 v121, v33, s63, v121
	v_pk_fma_f16 v26, v34, s96, v26
	v_pk_fma_f16 v27, v35, s97, v27
	v_pk_fma_f16 v28, v36, s98, v28
	v_pk_fma_f16 v29, v37, s99, v29
	s_waitcnt lgkmcnt(2)
	v_pk_fma_f16 v118, v106, s64, v118
	v_pk_fma_f16 v119, v107, s65, v119
	v_pk_fma_f16 v120, v108, s66, v120
	v_pk_fma_f16 v121, v109, s67, v121
	v_pk_fma_f16 v26, v110, s8, v26
	v_pk_fma_f16 v27, v111, s9, v27
	v_pk_fma_f16 v28, v112, s10, v28
	v_pk_fma_f16 v29, v113, s11, v29
	s_waitcnt lgkmcnt(0)
	v_pk_fma_f16 v26, v122, s12, v26
	v_pk_fma_f16 v27, v123, s13, v27
	v_pk_fma_f16 v28, v124, s14, v28
	v_pk_fma_f16 v29, v125, s15, v29
	v_pk_fma_f16 v109, v114, s68, v118
	v_pk_fma_f16 v123, v115, s69, v119
	v_pk_fma_f16 v122, v116, s70, v120
	v_pk_fma_f16 v105, v117, s71, v121
	s_add_u32 s16, s20, s0
	s_addc_u32 s17, s21, s1
	s_load_dwordx8 s[36:43], s[16:17], 0x16d80
	s_load_dwordx8 s[44:51], s[16:17], 0x16da0
	s_load_dwordx8 s[52:59], s[16:17], 0x16dc0
	s_load_dwordx8 s[60:67], s[16:17], 0x16de0
	s_load_dwordx4 s[68:71], s[16:17], 0x16e00
	s_load_dwordx8 s[72:79], s[16:17], 0x16fc0
	s_load_dwordx8 s[80:87], s[16:17], 0x16fe0
	s_load_dwordx8 s[88:95], s[16:17], 0x17000
	s_load_dwordx4 s[96:99], s[16:17], 0x17020
	s_load_dwordx8 s[8:15], s[16:17], 0x17030
	v_mov_b64_e32 v[114:115], s[22:23]
	v_fma_mix_f32 v106, |v109|, s31, v104 op_sel_hi:[1,0,0]
	v_fma_mix_f32 v107, |v109|, s31, v104 op_sel:[1,0,0] op_sel_hi:[1,0,0]
	v_rcp_f32_e32 v106, v106
	v_rcp_f32_e32 v107, v107
	v_fma_mix_f32 v110, v109, s100, 0 op_sel_hi:[1,0,0]
	v_fma_mix_f32 v111, v109, s100, 0 op_sel:[1,0,0] op_sel_hi:[1,0,0]
	v_mul_f32_e64 v110, v110, -v110
	v_mul_f32_e64 v111, v111, -v111
	v_pk_fma_f32 v[116:117], v[106:107], s[24:25], v[114:115] op_sel_hi:[1,0,0]
	v_exp_f32_e32 v110, v110
	v_pk_fma_f32 v[116:117], v[116:117], v[106:107], s[26:27] op_sel_hi:[1,1,0]
	v_exp_f32_e32 v111, v111
	v_pk_fma_f32 v[116:117], v[116:117], v[106:107], s[28:29] op_sel_hi:[1,1,0]
	v_pk_max_f16 v112, v109, 0
	v_pk_fma_f32 v[116:117], v[116:117], v[106:107], s[30:31] op_sel_hi:[1,1,0]
	v_pk_mul_f32 v[106:107], v[106:107], v[116:117]
	v_pk_mul_f32 v[106:107], v[110:111], v[106:107]
	v_fma_mixlo_f16 v109, -|v109|, v106, v112 op_sel_hi:[1,0,1]
	v_fma_mixhi_f16 v109, -|v109|, v107, v112 op_sel:[1,0,1] op_sel_hi:[1,0,1]
	v_fma_mix_f32 v106, |v123|, s31, v104 op_sel_hi:[1,0,0]
	v_fma_mix_f32 v107, |v123|, s31, v104 op_sel:[1,0,0] op_sel_hi:[1,0,0]
	v_rcp_f32_e32 v106, v106
	v_rcp_f32_e32 v107, v107
	v_fma_mix_f32 v110, v123, s100, 0 op_sel_hi:[1,0,0]
	v_fma_mix_f32 v111, v123, s100, 0 op_sel:[1,0,0] op_sel_hi:[1,0,0]
	v_mul_f32_e64 v110, v110, -v110
	v_mul_f32_e64 v111, v111, -v111
	v_pk_fma_f32 v[116:117], v[106:107], s[24:25], v[114:115] op_sel_hi:[1,0,0]
	v_exp_f32_e32 v110, v110
	v_pk_fma_f32 v[116:117], v[116:117], v[106:107], s[26:27] op_sel_hi:[1,1,0]
	v_exp_f32_e32 v111, v111
	v_pk_fma_f32 v[116:117], v[116:117], v[106:107], s[28:29] op_sel_hi:[1,1,0]
	v_pk_max_f16 v112, v123, 0
	v_pk_fma_f32 v[116:117], v[116:117], v[106:107], s[30:31] op_sel_hi:[1,1,0]
	v_pk_mul_f32 v[106:107], v[106:107], v[116:117]
	v_pk_mul_f32 v[106:107], v[110:111], v[106:107]
	v_fma_mixlo_f16 v123, -|v123|, v106, v112 op_sel_hi:[1,0,1]
	v_fma_mixhi_f16 v123, -|v123|, v107, v112 op_sel:[1,0,1] op_sel_hi:[1,0,1]
	v_fma_mix_f32 v106, |v122|, s31, v104 op_sel_hi:[1,0,0]
	v_fma_mix_f32 v107, |v122|, s31, v104 op_sel:[1,0,0] op_sel_hi:[1,0,0]
	v_rcp_f32_e32 v106, v106
	v_rcp_f32_e32 v107, v107
	v_fma_mix_f32 v110, v122, s100, 0 op_sel_hi:[1,0,0]
	v_fma_mix_f32 v111, v122, s100, 0 op_sel:[1,0,0] op_sel_hi:[1,0,0]
	v_mul_f32_e64 v110, v110, -v110
	v_mul_f32_e64 v111, v111, -v111
	v_pk_fma_f32 v[116:117], v[106:107], s[24:25], v[114:115] op_sel_hi:[1,0,0]
	v_exp_f32_e32 v110, v110
	v_pk_fma_f32 v[116:117], v[116:117], v[106:107], s[26:27] op_sel_hi:[1,1,0]
	v_exp_f32_e32 v111, v111
	v_pk_fma_f32 v[116:117], v[116:117], v[106:107], s[28:29] op_sel_hi:[1,1,0]
	v_pk_max_f16 v112, v122, 0
	v_pk_fma_f32 v[116:117], v[116:117], v[106:107], s[30:31] op_sel_hi:[1,1,0]
	v_pk_mul_f32 v[106:107], v[106:107], v[116:117]
	v_pk_mul_f32 v[106:107], v[110:111], v[106:107]
	v_fma_mixlo_f16 v122, -|v122|, v106, v112 op_sel_hi:[1,0,1]
	v_fma_mixhi_f16 v122, -|v122|, v107, v112 op_sel:[1,0,1] op_sel_hi:[1,0,1]
	v_fma_mix_f32 v106, |v105|, s31, v104 op_sel_hi:[1,0,0]
	v_fma_mix_f32 v107, |v105|, s31, v104 op_sel:[1,0,0] op_sel_hi:[1,0,0]
	v_rcp_f32_e32 v106, v106
	v_rcp_f32_e32 v107, v107
	v_fma_mix_f32 v110, v105, s100, 0 op_sel_hi:[1,0,0]
	v_fma_mix_f32 v111, v105, s100, 0 op_sel:[1,0,0] op_sel_hi:[1,0,0]
	v_mul_f32_e64 v110, v110, -v110
	v_mul_f32_e64 v111, v111, -v111
	v_pk_fma_f32 v[116:117], v[106:107], s[24:25], v[114:115] op_sel_hi:[1,0,0]
	v_exp_f32_e32 v110, v110
	v_pk_fma_f32 v[116:117], v[116:117], v[106:107], s[26:27] op_sel_hi:[1,1,0]
	v_exp_f32_e32 v111, v111
	v_pk_fma_f32 v[116:117], v[116:117], v[106:107], s[28:29] op_sel_hi:[1,1,0]
	v_pk_max_f16 v112, v105, 0
	v_pk_fma_f32 v[116:117], v[116:117], v[106:107], s[30:31] op_sel_hi:[1,1,0]
	v_pk_mul_f32 v[106:107], v[106:107], v[116:117]
	v_pk_mul_f32 v[106:107], v[110:111], v[106:107]
	v_fma_mixlo_f16 v105, -|v105|, v106, v112 op_sel_hi:[1,0,1]
	v_fma_mixhi_f16 v105, -|v105|, v107, v112 op_sel:[1,0,1] op_sel_hi:[1,0,1]
	v_pk_mul_f16 v26, v26, v109
	v_pk_mul_f16 v27, v27, v123
	v_pk_mul_f16 v28, v28, v122
	s_nop 0
	v_pk_mul_f16 v29, v29, v105
	v_add_u32_e32 v30, s25, v78
	ds_write_b128 v30, v[26:29]
	s_waitcnt vmcnt(0)
	ds_write_b128 v39, v[22:25]
	s_and_saveexec_b64 s[32:33], s[4:5]
	s_cbranch_execz .LBB4_36
	ds_write_b128 v39, v[18:21] offset:8192
	s_branch .LBB4_36
